# forgetting-attention loops: role A stages its K/V rows behind the compute interval like role B and the second workgroup barrier of each tile is dropped
# baseline (speedup 1.0000x reference)
.LBB0_530:
	s_and_b64 vcc, exec, s[12:13]
	s_cbranch_vccnz .LBB0_534
	v_add_u32_e32 v246, 0, v109
	s_waitcnt vmcnt(3)
	ds_write_b128 v100, v[16:19] offset:16384
	s_waitcnt vmcnt(2)
	ds_write_b128 v124, v[20:23] offset:16384
	s_waitcnt vmcnt(1)
	ds_write_b128 v246, v[24:27] offset:32768
	v_add_u32_e32 v246, 0, v112
	s_waitcnt vmcnt(0)
	ds_write_b128 v246, v[28:31] offset:32768

.LBB0_532:
	v_add_u32_e32 v152, s14, v151
	v_add_u32_e32 v64, 0x17d00, v152
	v_add_u32_e32 v65, 0x17d10, v152
	ds_read_b128 v[96:99], v64
	ds_read_b128 v[92:95], v65
	v_add_u32_e32 v64, 0x17d80, v152
	v_add_u32_e32 v65, 0x17d90, v152
	ds_read_b128 v[88:91], v64
	ds_read_b128 v[66:69], v65
	s_waitcnt lgkmcnt(0)
	s_waitcnt lgkmcnt(0)
	s_and_b64 vcc, exec, s[12:13]
	s_cbranch_vccnz .LBB0_536
	s_add_i32 s18, s16, 1
	s_cmp_lt_u32 s17, s68
	s_cselect_b32 s18, s18, 0
	s_mul_i32 s18, s18, 0x178000
	s_add_u32 s18, s0, s18
	s_addc_u32 s19, s1, 0
	s_waitcnt vmcnt(3)
	v_lshl_add_u64 v[16:17], s[18:19], 0, v[104:105]
	s_add_i32 s18, s16, 2
	s_mul_i32 s18, s18, 0x178000
	s_add_u32 s18, s52, s18
	s_waitcnt vmcnt(2)
	v_add_co_u32_e32 v20, vcc, 0xbc000, v16
	s_addc_u32 s19, s53, 0
	s_nop 0
	v_addc_co_u32_e32 v21, vcc, 0, v17, vcc
	s_waitcnt vmcnt(1)
	v_lshl_add_u64 v[24:25], s[18:19], 0, v[104:105]
	s_waitcnt vmcnt(0)
	v_add_co_u32_e32 v28, vcc, 0xbc000, v24
	global_load_dwordx4 v[16:19], v[16:17], off
	s_nop 0
	global_load_dwordx4 v[20:23], v[20:21], off
	v_addc_co_u32_e32 v29, vcc, 0, v25, vcc
	global_load_dwordx4 v[24:27], v[24:25], off
	s_nop 0
	global_load_dwordx4 v[28:31], v[28:29], off

.LBB0_538:
	s_and_b64 vcc, exec, s[12:13]
	s_cbranch_vccnz .LBB0_542
	v_add_u32_e32 v246, 0, v109
	s_waitcnt vmcnt(3)
	ds_write_b128 v100, v[16:19]
	s_waitcnt vmcnt(2)
	ds_write_b128 v124, v[20:23]
	s_waitcnt vmcnt(1)
	ds_write_b128 v246, v[24:27] offset:49152
	v_add_u32_e32 v246, 0, v112
	s_waitcnt vmcnt(0)
	ds_write_b128 v246, v[28:31] offset:49152

.LBB0_540:
	v_add_u32_e32 v72, 0x17c00, v152
	v_add_u32_e32 v73, 0x17c10, v152
	ds_read_b128 v[92:95], v72
	ds_read_b128 v[88:91], v73
	v_add_u32_e32 v72, 0x17c80, v152
	v_add_u32_e32 v73, 0x17c90, v152
	ds_read_b128 v[84:87], v72
	ds_read_b128 v[72:75], v73
	v_add_f32_e32 v96, v150, v96
	v_add_f32_e32 v96, v97, v96
	v_add_f32_e32 v96, v98, v96
	v_add_f32_e32 v96, v99, v96
	v_add_f32_e32 v96, v153, v96
	v_add_f32_e32 v96, v154, v96
	v_add_f32_e32 v96, v155, v96
	v_add_f32_e32 v96, v156, v96
	v_add_f32_e32 v96, v157, v96
	v_add_f32_e32 v96, v158, v96
	v_add_f32_e32 v96, v159, v96
	s_waitcnt lgkmcnt(3)
	v_sub_f32_e32 v92, v127, v92
	v_add_f32_e32 v96, v160, v96
	v_add_f32_e32 v80, v80, v92
	v_sub_f32_e32 v92, v127, v93
	v_add_f32_e32 v96, v161, v96
	v_exp_f32_e32 v80, v80
	v_add_f32_e32 v81, v81, v92
	v_sub_f32_e32 v92, v127, v94
	v_add_f32_e32 v96, v162, v96
	v_exp_f32_e32 v81, v81
	v_add_f32_e32 v82, v82, v92
	v_sub_f32_e32 v92, v127, v95
	v_add_f32_e32 v96, v163, v96
	v_exp_f32_e32 v82, v82
	v_add_f32_e32 v83, v83, v92
	s_waitcnt lgkmcnt(2)
	v_sub_f32_e32 v88, v127, v88
	v_add_f32_e32 v96, v164, v96
	v_exp_f32_e32 v83, v83
	v_add_f32_e32 v76, v76, v88
	v_sub_f32_e32 v88, v127, v89
	v_add_f32_e32 v92, v96, v80
	v_exp_f32_e32 v76, v76
	v_add_f32_e32 v77, v77, v88
	v_sub_f32_e32 v88, v127, v90
	v_add_f32_e32 v92, v81, v92
	v_exp_f32_e32 v77, v77
	v_add_f32_e32 v78, v78, v88
	v_sub_f32_e32 v88, v127, v91
	v_add_f32_e32 v92, v82, v92
	v_exp_f32_e32 v78, v78
	v_add_f32_e32 v79, v79, v88
	s_waitcnt lgkmcnt(1)
	v_sub_f32_e32 v84, v127, v84
	v_add_f32_e32 v92, v83, v92
	v_exp_f32_e32 v79, v79
	v_add_f32_e32 v64, v64, v84
	v_sub_f32_e32 v84, v127, v85
	s_waitcnt lgkmcnt(0)
	v_sub_f32_e32 v72, v127, v72
	v_add_f32_e32 v88, v76, v92
	v_exp_f32_e32 v64, v64
	v_add_f32_e32 v65, v65, v84
	v_sub_f32_e32 v84, v127, v86
	v_add_f32_e32 v68, v68, v72
	v_add_f32_e32 v88, v77, v88
	v_exp_f32_e32 v65, v65
	v_add_f32_e32 v66, v66, v84
	v_sub_f32_e32 v84, v127, v87
	v_exp_f32_e32 v72, v68
	v_sub_f32_e32 v68, v127, v73
	v_add_f32_e32 v88, v78, v88
	v_exp_f32_e32 v66, v66
	v_add_f32_e32 v67, v67, v84
	v_add_f32_e32 v68, v69, v68
	v_add_f32_e32 v88, v79, v88
	v_exp_f32_e32 v67, v67
	v_exp_f32_e32 v73, v68
	v_sub_f32_e32 v68, v127, v74
	v_add_f32_e32 v84, v64, v88
	v_add_f32_e32 v68, v70, v68
	v_add_f32_e32 v84, v65, v84
	v_exp_f32_e32 v74, v68
	v_sub_f32_e32 v68, v127, v75
	v_add_f32_e32 v84, v66, v84
	v_add_f32_e32 v68, v71, v68
	v_add_f32_e32 v84, v67, v84
	v_exp_f32_e32 v75, v68
	v_add_f32_e32 v68, v72, v84
	v_add_f32_e32 v68, v73, v68
	v_add_f32_e32 v68, v74, v68
	v_add_f32_e32 v150, v75, v68
	v_cvt_pk_bf16_f32 v68, v80, v81
	v_cvt_pk_bf16_f32 v69, v82, v83
	v_cvt_pk_bf16_f32 v70, v76, v77
	v_cvt_pk_bf16_f32 v71, v78, v79
	v_cvt_pk_bf16_f32 v64, v64, v65
	v_cvt_pk_bf16_f32 v65, v66, v67
	v_cvt_pk_bf16_f32 v66, v72, v73
	v_cvt_pk_bf16_f32 v67, v74, v75
	s_waitcnt lgkmcnt(0)
	s_add_i32 s18, s17, 2
	s_add_i32 s16, s16, -2
	s_add_i32 s15, s15, 0xffd10000
	s_addk_i32 s14, 0xfe00
	s_cmp_ge_u32 s17, s68
	s_cbranch_scc1 .LBB0_544
	s_mov_b32 s17, s18
	s_and_b64 vcc, exec, s[12:13]
	s_cbranch_vccz .LBB0_527
	s_branch .LBB0_528

.LBB0_571:
	ds_read_b128 v[96:99], v151 offset:256
	ds_read_b128 v[92:95], v151 offset:272
	ds_read_b128 v[88:91], v151 offset:384
	ds_read_b128 v[66:69], v151 offset:400
	s_waitcnt lgkmcnt(0)
	s_waitcnt lgkmcnt(0)
	s_and_b64 vcc, exec, s[12:13]
	s_cbranch_vccnz .LBB0_575
	s_add_i32 s20, s18, 1
	s_cmp_lt_u32 s19, s16
	s_cselect_b32 s20, s20, 0
	s_mul_i32 s20, s20, 0x178000
	s_add_u32 s20, s0, s20
	s_addc_u32 s21, s1, 0
	s_waitcnt vmcnt(3)
	v_lshl_add_u64 v[16:17], s[20:21], 0, v[104:105]
	s_add_i32 s20, s18, 2
	s_mul_i32 s20, s20, 0x178000
	s_add_u32 s20, s52, s20
	s_waitcnt vmcnt(2)
	v_add_co_u32_e32 v20, vcc, 0xbc000, v16
	s_addc_u32 s21, s53, 0
	s_nop 0
	v_addc_co_u32_e32 v21, vcc, 0, v17, vcc
	s_waitcnt vmcnt(1)
	v_lshl_add_u64 v[24:25], s[20:21], 0, v[104:105]
	s_waitcnt vmcnt(0)
	v_add_co_u32_e32 v28, vcc, 0xbc000, v24
	global_load_dwordx4 v[16:19], v[16:17], off
	s_nop 0
	global_load_dwordx4 v[20:23], v[20:21], off
	v_addc_co_u32_e32 v29, vcc, 0, v25, vcc
	global_load_dwordx4 v[24:27], v[24:25], off
	s_nop 0
	global_load_dwordx4 v[28:31], v[28:29], off

.LBB0_579:
	ds_read_b128 v[92:95], v151
	ds_read_b128 v[88:91], v151 offset:16
	ds_read_b128 v[84:87], v151 offset:128
	ds_read_b128 v[72:75], v151 offset:144
	v_add_f32_e32 v96, v150, v96
	v_add_f32_e32 v96, v97, v96
	v_add_f32_e32 v96, v98, v96
	v_add_f32_e32 v96, v99, v96
	v_add_f32_e32 v96, v152, v96
	v_add_f32_e32 v96, v153, v96
	v_add_f32_e32 v96, v154, v96
	v_add_f32_e32 v96, v155, v96
	v_add_f32_e32 v96, v156, v96
	v_add_f32_e32 v96, v157, v96
	v_add_f32_e32 v96, v158, v96
	s_waitcnt lgkmcnt(3)
	v_sub_f32_e32 v92, v128, v92
	v_add_f32_e32 v96, v159, v96
	v_add_f32_e32 v80, v80, v92
	v_sub_f32_e32 v92, v128, v93
	v_add_f32_e32 v96, v160, v96
	v_exp_f32_e32 v80, v80
	v_add_f32_e32 v81, v81, v92
	v_sub_f32_e32 v92, v128, v94
	v_add_f32_e32 v96, v161, v96
	v_exp_f32_e32 v81, v81
	v_add_f32_e32 v82, v82, v92
	v_sub_f32_e32 v92, v128, v95
	v_add_f32_e32 v96, v162, v96
	v_exp_f32_e32 v82, v82
	v_add_f32_e32 v83, v83, v92
	s_waitcnt lgkmcnt(2)
	v_sub_f32_e32 v88, v128, v88
	v_add_f32_e32 v96, v163, v96
	v_exp_f32_e32 v83, v83
	v_add_f32_e32 v76, v76, v88
	v_sub_f32_e32 v88, v128, v89
	v_add_f32_e32 v92, v96, v80
	v_exp_f32_e32 v76, v76
	v_add_f32_e32 v77, v77, v88
	v_sub_f32_e32 v88, v128, v90
	v_add_f32_e32 v92, v81, v92
	v_exp_f32_e32 v77, v77
	v_add_f32_e32 v78, v78, v88
	v_sub_f32_e32 v88, v128, v91
	v_add_f32_e32 v92, v82, v92
	v_exp_f32_e32 v78, v78
	v_add_f32_e32 v79, v79, v88
	s_waitcnt lgkmcnt(1)
	v_sub_f32_e32 v84, v128, v84
	v_add_f32_e32 v92, v83, v92
	v_exp_f32_e32 v79, v79
	v_add_f32_e32 v64, v64, v84
	v_sub_f32_e32 v84, v128, v85
	s_waitcnt lgkmcnt(0)
	v_sub_f32_e32 v72, v128, v72
	v_add_f32_e32 v88, v76, v92
	v_exp_f32_e32 v64, v64
	v_add_f32_e32 v65, v65, v84
	v_sub_f32_e32 v84, v128, v86
	v_add_f32_e32 v68, v68, v72
	v_add_f32_e32 v88, v77, v88
	v_exp_f32_e32 v65, v65
	v_add_f32_e32 v66, v66, v84
	v_sub_f32_e32 v84, v128, v87
	v_exp_f32_e32 v72, v68
	v_sub_f32_e32 v68, v128, v73
	v_add_f32_e32 v88, v78, v88
	v_exp_f32_e32 v66, v66
	v_add_f32_e32 v67, v67, v84
	v_add_f32_e32 v68, v69, v68
	v_add_f32_e32 v88, v79, v88
	v_exp_f32_e32 v67, v67
	v_exp_f32_e32 v73, v68
	v_sub_f32_e32 v68, v128, v74
	v_add_f32_e32 v84, v64, v88
	v_add_f32_e32 v68, v70, v68
	v_add_f32_e32 v84, v65, v84
	v_exp_f32_e32 v74, v68
	v_sub_f32_e32 v68, v128, v75
	v_add_f32_e32 v84, v66, v84
	v_add_f32_e32 v68, v71, v68
	v_add_f32_e32 v84, v67, v84
	v_exp_f32_e32 v75, v68
	v_add_f32_e32 v68, v72, v84
	v_add_f32_e32 v68, v73, v68
	v_add_f32_e32 v68, v74, v68
	v_add_f32_e32 v150, v75, v68
	v_cvt_pk_bf16_f32 v68, v80, v81
	v_cvt_pk_bf16_f32 v69, v82, v83
	v_cvt_pk_bf16_f32 v70, v76, v77
	v_cvt_pk_bf16_f32 v71, v78, v79
	v_cvt_pk_bf16_f32 v64, v64, v65
	v_cvt_pk_bf16_f32 v65, v66, v67
	v_cvt_pk_bf16_f32 v66, v72, v73
	v_cvt_pk_bf16_f32 v67, v74, v75
	s_waitcnt lgkmcnt(0)
	s_add_i32 s20, s19, 2
	s_add_i32 s18, s18, -2
	s_add_i32 s17, s17, 0xffd10000
	s_cmp_ge_u32 s19, s16
	v_add_u32_e32 v151, 0xfffffe00, v151
	s_cbranch_scc1 .LBB0_583
	s_mov_b32 s19, s20
	s_and_b64 vcc, exec, s[12:13]
	s_cbranch_vccz .LBB0_566
	s_branch .LBB0_567

.LBB0_1921:
	s_and_b64 vcc, exec, s[8:9]
	s_cbranch_vccnz .LBB0_1925
	v_add_u32_e32 v246, 0, v109
	s_waitcnt vmcnt(3)
	ds_write_b128 v100, v[16:19] offset:16384
	s_waitcnt vmcnt(2)
	ds_write_b128 v124, v[20:23] offset:16384
	s_waitcnt vmcnt(1)
	ds_write_b128 v246, v[24:27] offset:32768
	v_add_u32_e32 v246, 0, v112
	s_waitcnt vmcnt(0)
	ds_write_b128 v246, v[28:31] offset:32768

.LBB0_1923:
	v_add_u32_e32 v152, s5, v151
	v_add_u32_e32 v64, 0x17d00, v152
	v_add_u32_e32 v65, 0x17d10, v152
	ds_read_b128 v[96:99], v64
	ds_read_b128 v[92:95], v65
	v_add_u32_e32 v64, 0x17d80, v152
	v_add_u32_e32 v65, 0x17d90, v152
	ds_read_b128 v[88:91], v64
	ds_read_b128 v[66:69], v65
	s_waitcnt lgkmcnt(0)
	s_waitcnt lgkmcnt(0)
	s_and_b64 vcc, exec, s[8:9]
	s_cbranch_vccnz .LBB0_1927
	s_add_i32 s13, s11, 1
	s_cmp_lt_u32 s12, s4
	s_cselect_b32 s13, s13, 0
	s_mul_i32 s13, s13, 0x178000
	s_add_u32 s14, s48, s13
	s_addc_u32 s15, s49, 0
	s_add_i32 s13, s11, 2
	s_mul_i32 s13, s13, 0x178000
	s_waitcnt vmcnt(3)
	v_lshl_add_u64 v[16:17], s[14:15], 0, v[104:105]
	s_add_u32 s14, s68, s13
	s_waitcnt vmcnt(2)
	v_add_co_u32_e32 v20, vcc, 0xbc000, v16
	s_addc_u32 s15, s69, 0
	s_nop 0
	v_addc_co_u32_e32 v21, vcc, 0, v17, vcc
	s_waitcnt vmcnt(1)
	v_lshl_add_u64 v[24:25], s[14:15], 0, v[104:105]
	s_waitcnt vmcnt(0)
	v_add_co_u32_e32 v28, vcc, 0xbc000, v24
	global_load_dwordx4 v[16:19], v[16:17], off
	s_nop 0
	global_load_dwordx4 v[20:23], v[20:21], off
	v_addc_co_u32_e32 v29, vcc, 0, v25, vcc
	global_load_dwordx4 v[24:27], v[24:25], off
	s_nop 0
	global_load_dwordx4 v[28:31], v[28:29], off

.LBB0_1929:
	s_and_b64 vcc, exec, s[8:9]
	s_cbranch_vccnz .LBB0_1933
	v_add_u32_e32 v246, 0, v109
	s_waitcnt vmcnt(3)
	ds_write_b128 v100, v[16:19]
	s_waitcnt vmcnt(2)
	ds_write_b128 v124, v[20:23]
	s_waitcnt vmcnt(1)
	ds_write_b128 v246, v[24:27] offset:49152
	v_add_u32_e32 v246, 0, v112
	s_waitcnt vmcnt(0)
	ds_write_b128 v246, v[28:31] offset:49152

.LBB0_1931:
	v_add_u32_e32 v72, 0x17c00, v152
	v_add_u32_e32 v73, 0x17c10, v152
	ds_read_b128 v[92:95], v72
	ds_read_b128 v[88:91], v73
	v_add_u32_e32 v72, 0x17c80, v152
	v_add_u32_e32 v73, 0x17c90, v152
	ds_read_b128 v[84:87], v72
	ds_read_b128 v[72:75], v73
	v_add_f32_e32 v96, v150, v96
	v_add_f32_e32 v96, v97, v96
	v_add_f32_e32 v96, v98, v96
	v_add_f32_e32 v96, v99, v96
	v_add_f32_e32 v96, v153, v96
	v_add_f32_e32 v96, v154, v96
	v_add_f32_e32 v96, v155, v96
	v_add_f32_e32 v96, v156, v96
	v_add_f32_e32 v96, v157, v96
	v_add_f32_e32 v96, v158, v96
	v_add_f32_e32 v96, v159, v96
	s_waitcnt lgkmcnt(3)
	v_sub_f32_e32 v92, v127, v92
	v_add_f32_e32 v96, v160, v96
	v_add_f32_e32 v80, v80, v92
	v_sub_f32_e32 v92, v127, v93
	v_add_f32_e32 v96, v161, v96
	v_exp_f32_e32 v80, v80
	v_add_f32_e32 v81, v81, v92
	v_sub_f32_e32 v92, v127, v94
	v_add_f32_e32 v96, v162, v96
	v_exp_f32_e32 v81, v81
	v_add_f32_e32 v82, v82, v92
	v_sub_f32_e32 v92, v127, v95
	v_add_f32_e32 v96, v163, v96
	v_exp_f32_e32 v82, v82
	v_add_f32_e32 v83, v83, v92
	s_waitcnt lgkmcnt(2)
	v_sub_f32_e32 v88, v127, v88
	v_add_f32_e32 v96, v164, v96
	v_exp_f32_e32 v83, v83
	v_add_f32_e32 v76, v76, v88
	v_sub_f32_e32 v88, v127, v89
	v_add_f32_e32 v92, v96, v80
	v_exp_f32_e32 v76, v76
	v_add_f32_e32 v77, v77, v88
	v_sub_f32_e32 v88, v127, v90
	v_add_f32_e32 v92, v81, v92
	v_exp_f32_e32 v77, v77
	v_add_f32_e32 v78, v78, v88
	v_sub_f32_e32 v88, v127, v91
	v_add_f32_e32 v92, v82, v92
	v_exp_f32_e32 v78, v78
	v_add_f32_e32 v79, v79, v88
	s_waitcnt lgkmcnt(1)
	v_sub_f32_e32 v84, v127, v84
	v_add_f32_e32 v92, v83, v92
	v_exp_f32_e32 v79, v79
	v_add_f32_e32 v64, v64, v84
	v_sub_f32_e32 v84, v127, v85
	s_waitcnt lgkmcnt(0)
	v_sub_f32_e32 v72, v127, v72
	v_add_f32_e32 v88, v76, v92
	v_exp_f32_e32 v64, v64
	v_add_f32_e32 v65, v65, v84
	v_sub_f32_e32 v84, v127, v86
	v_add_f32_e32 v68, v68, v72
	v_add_f32_e32 v88, v77, v88
	v_exp_f32_e32 v65, v65
	v_add_f32_e32 v66, v66, v84
	v_sub_f32_e32 v84, v127, v87
	v_exp_f32_e32 v72, v68
	v_sub_f32_e32 v68, v127, v73
	v_add_f32_e32 v88, v78, v88
	v_exp_f32_e32 v66, v66
	v_add_f32_e32 v67, v67, v84
	v_add_f32_e32 v68, v69, v68
	v_add_f32_e32 v88, v79, v88
	v_exp_f32_e32 v67, v67
	v_exp_f32_e32 v73, v68
	v_sub_f32_e32 v68, v127, v74
	v_add_f32_e32 v84, v64, v88
	v_add_f32_e32 v68, v70, v68
	v_add_f32_e32 v84, v65, v84
	v_exp_f32_e32 v74, v68
	v_sub_f32_e32 v68, v127, v75
	v_add_f32_e32 v84, v66, v84
	v_add_f32_e32 v68, v71, v68
	v_add_f32_e32 v84, v67, v84
	v_exp_f32_e32 v75, v68
	v_add_f32_e32 v68, v72, v84
	v_add_f32_e32 v68, v73, v68
	v_add_f32_e32 v68, v74, v68
	v_add_f32_e32 v150, v75, v68
	v_cvt_pk_bf16_f32 v68, v80, v81
	v_cvt_pk_bf16_f32 v69, v82, v83
	v_cvt_pk_bf16_f32 v70, v76, v77
	v_cvt_pk_bf16_f32 v71, v78, v79
	v_cvt_pk_bf16_f32 v64, v64, v65
	v_cvt_pk_bf16_f32 v65, v66, v67
	v_cvt_pk_bf16_f32 v66, v72, v73
	v_cvt_pk_bf16_f32 v67, v74, v75
	s_waitcnt lgkmcnt(0)
	s_add_i32 s13, s12, 2
	s_add_i32 s11, s11, -2
	s_add_i32 s10, s10, 0xffd10000
	s_addk_i32 s5, 0xfe00
	s_cmp_ge_u32 s12, s4
	s_cbranch_scc1 .LBB0_1935
	s_mov_b32 s12, s13
	s_and_b64 vcc, exec, s[8:9]
	s_cbranch_vccz .LBB0_1918
	s_branch .LBB0_1919

.LBB0_1962:
	ds_read_b128 v[96:99], v151 offset:256
	ds_read_b128 v[92:95], v151 offset:272
	ds_read_b128 v[88:91], v151 offset:384
	ds_read_b128 v[66:69], v151 offset:400
	s_waitcnt lgkmcnt(0)
	s_waitcnt lgkmcnt(0)
	s_and_b64 vcc, exec, s[8:9]
	s_cbranch_vccnz .LBB0_1966
	s_add_i32 s13, s5, 1
	s_cmp_lt_u32 s12, s0
	s_cselect_b32 s13, s13, 0
	s_mul_i32 s13, s13, 0x178000
	s_add_u32 s14, s48, s13
	s_addc_u32 s15, s49, 0
	s_add_i32 s13, s5, 2
	s_mul_i32 s13, s13, 0x178000
	s_waitcnt vmcnt(3)
	v_lshl_add_u64 v[16:17], s[14:15], 0, v[104:105]
	s_add_u32 s14, s68, s13
	s_waitcnt vmcnt(2)
	v_add_co_u32_e32 v20, vcc, 0xbc000, v16
	s_addc_u32 s15, s69, 0
	s_nop 0
	v_addc_co_u32_e32 v21, vcc, 0, v17, vcc
	s_waitcnt vmcnt(1)
	v_lshl_add_u64 v[24:25], s[14:15], 0, v[104:105]
	s_waitcnt vmcnt(0)
	v_add_co_u32_e32 v28, vcc, 0xbc000, v24
	global_load_dwordx4 v[16:19], v[16:17], off
	s_nop 0
	global_load_dwordx4 v[20:23], v[20:21], off
	v_addc_co_u32_e32 v29, vcc, 0, v25, vcc
	global_load_dwordx4 v[24:27], v[24:25], off
	s_nop 0
	global_load_dwordx4 v[28:31], v[28:29], off

.LBB0_1970:
	ds_read_b128 v[92:95], v151
	ds_read_b128 v[88:91], v151 offset:16
	ds_read_b128 v[84:87], v151 offset:128
	ds_read_b128 v[72:75], v151 offset:144
	v_add_f32_e32 v96, v150, v96
	v_add_f32_e32 v96, v97, v96
	v_add_f32_e32 v96, v98, v96
	v_add_f32_e32 v96, v99, v96
	v_add_f32_e32 v96, v152, v96
	v_add_f32_e32 v96, v153, v96
	v_add_f32_e32 v96, v154, v96
	v_add_f32_e32 v96, v155, v96
	v_add_f32_e32 v96, v156, v96
	v_add_f32_e32 v96, v157, v96
	v_add_f32_e32 v96, v158, v96
	s_waitcnt lgkmcnt(3)
	v_sub_f32_e32 v92, v128, v92
	v_add_f32_e32 v96, v159, v96
	v_add_f32_e32 v80, v80, v92
	v_sub_f32_e32 v92, v128, v93
	v_add_f32_e32 v96, v160, v96
	v_exp_f32_e32 v80, v80
	v_add_f32_e32 v81, v81, v92
	v_sub_f32_e32 v92, v128, v94
	v_add_f32_e32 v96, v161, v96
	v_exp_f32_e32 v81, v81
	v_add_f32_e32 v82, v82, v92
	v_sub_f32_e32 v92, v128, v95
	v_add_f32_e32 v96, v162, v96
	v_exp_f32_e32 v82, v82
	v_add_f32_e32 v83, v83, v92
	s_waitcnt lgkmcnt(2)
	v_sub_f32_e32 v88, v128, v88
	v_add_f32_e32 v96, v163, v96
	v_exp_f32_e32 v83, v83
	v_add_f32_e32 v76, v76, v88
	v_sub_f32_e32 v88, v128, v89
	v_add_f32_e32 v92, v96, v80
	v_exp_f32_e32 v76, v76
	v_add_f32_e32 v77, v77, v88
	v_sub_f32_e32 v88, v128, v90
	v_add_f32_e32 v92, v81, v92
	v_exp_f32_e32 v77, v77
	v_add_f32_e32 v78, v78, v88
	v_sub_f32_e32 v88, v128, v91
	v_add_f32_e32 v92, v82, v92
	v_exp_f32_e32 v78, v78
	v_add_f32_e32 v79, v79, v88
	s_waitcnt lgkmcnt(1)
	v_sub_f32_e32 v84, v128, v84
	v_add_f32_e32 v92, v83, v92
	v_exp_f32_e32 v79, v79
	v_add_f32_e32 v64, v64, v84
	v_sub_f32_e32 v84, v128, v85
	s_waitcnt lgkmcnt(0)
	v_sub_f32_e32 v72, v128, v72
	v_add_f32_e32 v88, v76, v92
	v_exp_f32_e32 v64, v64
	v_add_f32_e32 v65, v65, v84
	v_sub_f32_e32 v84, v128, v86
	v_add_f32_e32 v68, v68, v72
	v_add_f32_e32 v88, v77, v88
	v_exp_f32_e32 v65, v65
	v_add_f32_e32 v66, v66, v84
	v_sub_f32_e32 v84, v128, v87
	v_exp_f32_e32 v72, v68
	v_sub_f32_e32 v68, v128, v73
	v_add_f32_e32 v88, v78, v88
	v_exp_f32_e32 v66, v66
	v_add_f32_e32 v67, v67, v84
	v_add_f32_e32 v68, v69, v68
	v_add_f32_e32 v88, v79, v88
	v_exp_f32_e32 v67, v67
	v_exp_f32_e32 v73, v68
	v_sub_f32_e32 v68, v128, v74
	v_add_f32_e32 v84, v64, v88
	v_add_f32_e32 v68, v70, v68
	v_add_f32_e32 v84, v65, v84
	v_exp_f32_e32 v74, v68
	v_sub_f32_e32 v68, v128, v75
	v_add_f32_e32 v84, v66, v84
	v_add_f32_e32 v68, v71, v68
	v_add_f32_e32 v84, v67, v84
	v_exp_f32_e32 v75, v68
	v_add_f32_e32 v68, v72, v84
	v_add_f32_e32 v68, v73, v68
	v_add_f32_e32 v68, v74, v68
	v_add_f32_e32 v150, v75, v68
	v_cvt_pk_bf16_f32 v68, v80, v81
	v_cvt_pk_bf16_f32 v69, v82, v83
	v_cvt_pk_bf16_f32 v70, v76, v77
	v_cvt_pk_bf16_f32 v71, v78, v79
	v_cvt_pk_bf16_f32 v64, v64, v65
	v_cvt_pk_bf16_f32 v65, v66, v67
	v_cvt_pk_bf16_f32 v66, v72, v73
	v_cvt_pk_bf16_f32 v67, v74, v75
	s_waitcnt lgkmcnt(0)
	s_add_i32 s13, s12, 2
	s_add_i32 s5, s5, -2
	s_add_i32 s4, s4, 0xffd10000
	s_cmp_ge_u32 s12, s0
	v_add_u32_e32 v151, 0xfffffe00, v151
	s_cbranch_scc1 .LBB0_1974
	s_mov_b32 s12, s13
	s_and_b64 vcc, exec, s[8:9]
	s_cbranch_vccz .LBB0_1957
	s_branch .LBB0_1958
